# indexer head loop: removed vmcnt waits that only covered the next item's Q DMA (K fragments are already drained before the barrier)
# baseline (speedup 1.0000x reference)
; #define LAS __attribute__((address_space(3)))
; #define IDX_ACC(cc, jj) do { float s0 = fmaf(wh, __builtin_fabsf(cc[0]), sacc[jj][0]); sacc[jj][0] = s0; \
;                             _Pragma("unroll") for (int r = 1; r < 16; ++r) { float a_ = sacc[jj][r]; asm("v_fma_f32 %0, %1, |%2|, %0" : "+v"(a_) : "v"(wh), "v"(cc[r]), "v"(s0)); sacc[jj][r] = a_; } } while (0)
; __global__ void __launch_bounds__(NTHREADS, 2) mega_fwd(Args args) {
;     ...
;                 for (int h = 0; h < NIH; ++h) {
;                     bf16x8 qf[4];
; #pragma unroll
;                     for (int ks = 0; ks < 4; ++ks) qf[ks] = *(const LAS bf16x8*)(Qs + (((h * 4 + ks) * 2 + hi5) * 32 + r32) * 16);
;                     const float wh = Ws[h * 32 + r32];
; #pragma unroll
;                     for (int jp = 0; jp < 4; jp += 2) { f32x16 c0 = f32x16{}, c1 = f32x16{};
; #pragma unroll
;                         for (int ks = 0; ks < 4; ++ks) { c0 = __builtin_amdgcn_mfma_f32_32x32x16_bf16(kf[jp][ks], qf[ks], c0, 0, 0, 0); c1 = __builtin_amdgcn_mfma_f32_32x32x16_bf16(kf[jp + 1][ks], qf[ks], c1, 0, 0, 0); }
;                         __builtin_amdgcn_sched_barrier(0);
;     ...
;                         IDX_ACC(c0, jp); IDX_ACC(c1, jp + 1);
.LBB0_656:
	v_add_u32_e32 v58, s7, v233
	ds_read_b128 v[42:45], v58
	ds_read_b128 v[46:49], v58 offset:1024
	ds_read_b128 v[50:53], v58 offset:2048
	ds_read_b128 v[54:57], v58 offset:3072
	s_nop 4
	v_add_u32_e32 v2, 0xffffff80, v234
	ds_read_b32 v235, v2
	s_waitcnt lgkmcnt(4)
	v_mfma_f32_32x32x16_bf16 v[10:25], v[66:69], v[42:45], 0
	s_waitcnt lgkmcnt(3)
	v_mfma_f32_32x32x16_bf16 v[10:25], v[70:73], v[46:49], v[10:25]
	s_waitcnt lgkmcnt(2)
	v_mfma_f32_32x32x16_bf16 v[10:25], v[74:77], v[50:53], v[10:25]
	s_waitcnt lgkmcnt(1)
	v_mfma_f32_32x32x16_bf16 v[10:25], v[78:81], v[54:57], v[10:25]
	v_mfma_f32_32x32x16_bf16 v[26:41], v[82:85], v[42:45], 0
	s_waitcnt lgkmcnt(0)
	s_nop 8
	v_fma_f32 v206, v235, |v10|, v206
	v_fma_f32 v207, v235, |v11|, v207
	v_fma_f32 v208, v235, |v12|, v208
	v_fma_f32 v209, v235, |v13|, v209
	v_fma_f32 v210, v235, |v14|, v210
	v_fma_f32 v211, v235, |v15|, v211
	v_fma_f32 v212, v235, |v16|, v212
	v_mfma_f32_32x32x16_bf16 v[26:41], v[86:89], v[46:49], v[26:41]
	v_fma_f32 v213, v235, |v17|, v213
	v_fma_f32 v214, v235, |v18|, v214
	v_fma_f32 v215, v235, |v19|, v215
	v_fma_f32 v216, v235, |v20|, v216
	v_fma_f32 v217, v235, |v21|, v217
	v_fma_f32 v218, v235, |v22|, v218
	v_fma_f32 v219, v235, |v23|, v219
	v_mfma_f32_32x32x16_bf16 v[4:19], v[98:101], v[42:45], 0
	v_fma_f32 v220, v235, |v24|, v220
	v_fma_f32 v221, v235, |v25|, v221
	v_mfma_f32_32x32x16_bf16 v[26:41], v[90:93], v[50:53], v[26:41]
	v_mfma_f32_32x32x16_bf16 v[4:19], v[102:105], v[46:49], v[4:19]
	v_mfma_f32_32x32x16_bf16 v[26:41], v[94:97], v[54:57], v[26:41]
	v_mfma_f32_32x32x16_bf16 v[4:19], v[106:109], v[50:53], v[4:19]
	s_nop 9
	v_fma_f32 v190, v235, |v26|, v190
	v_fma_f32 v191, v235, |v27|, v191
	v_fma_f32 v192, v235, |v28|, v192
	v_fma_f32 v193, v235, |v29|, v193
	v_fma_f32 v194, v235, |v30|, v194
	v_fma_f32 v195, v235, |v31|, v195
	v_fma_f32 v196, v235, |v32|, v196
	v_fma_f32 v197, v235, |v33|, v197
	v_fma_f32 v198, v235, |v34|, v198
	v_fma_f32 v199, v235, |v35|, v199
	v_fma_f32 v200, v235, |v36|, v200
	v_fma_f32 v201, v235, |v37|, v201
	v_fma_f32 v202, v235, |v38|, v202
	v_fma_f32 v203, v235, |v39|, v203
	v_fma_f32 v204, v235, |v40|, v204
	v_fma_f32 v205, v235, |v41|, v205
	v_mfma_f32_32x32x16_bf16 v[4:19], v[114:117], v[54:57], v[4:19]
	v_mfma_f32_32x32x16_bf16 v[20:35], v[130:133], v[42:45], 0
	s_nop 9
	v_fma_f32 v188, v235, |v4|, v188
	v_fma_f32 v189, v235, |v5|, v189
	v_fma_f32 v186, v235, |v6|, v186
	v_fma_f32 v187, v235, |v7|, v187
	v_fma_f32 v184, v235, |v8|, v184
	v_fma_f32 v185, v235, |v9|, v185
	v_fma_f32 v182, v235, |v10|, v182
	v_mfma_f32_32x32x16_bf16 v[20:35], v[134:137], v[46:49], v[20:35]
	v_fma_f32 v183, v235, |v11|, v183
	v_fma_f32 v180, v235, |v12|, v180
	v_fma_f32 v181, v235, |v13|, v181
	v_fma_f32 v178, v235, |v14|, v178
	v_fma_f32 v179, v235, |v15|, v179
	v_fma_f32 v176, v235, |v16|, v176
	v_fma_f32 v177, v235, |v17|, v177
	v_mfma_f32_32x32x16_bf16 v[20:35], v[138:141], v[50:53], v[20:35]
	ds_read_b128 v[50:53], v58 offset:4096
	ds_read_b128 v[62:65], v58 offset:6144
	v_fma_f32 v174, v235, |v18|, v174
	v_fma_f32 v175, v235, |v19|, v175
	v_mfma_f32_32x32x16_bf16 v[20:35], v[142:145], v[54:57], v[20:35]
	ds_read_b128 v[54:57], v58 offset:5120
	ds_read_b128 v[58:61], v58 offset:7168
	s_waitcnt lgkmcnt(3)
	v_mfma_f32_32x32x16_bf16 v[2:17], v[66:69], v[50:53], 0
	s_nop 7
	v_fma_f32 v172, v235, |v20|, v172
	v_fma_f32 v173, v235, |v21|, v173
	v_fma_f32 v170, v235, |v22|, v170
	v_fma_f32 v171, v235, |v23|, v171
	v_fma_f32 v168, v235, |v24|, v168
	v_fma_f32 v169, v235, |v25|, v169
	v_fma_f32 v166, v235, |v26|, v166
	s_waitcnt lgkmcnt(1)
	v_mfma_f32_32x32x16_bf16 v[2:17], v[70:73], v[54:57], v[2:17]
	v_fma_f32 v167, v235, |v27|, v167
	v_fma_f32 v164, v235, |v28|, v164
	v_fma_f32 v165, v235, |v29|, v165
	v_fma_f32 v162, v235, |v30|, v162
	v_fma_f32 v163, v235, |v31|, v163
	v_fma_f32 v160, v235, |v32|, v160
	v_fma_f32 v161, v235, |v33|, v161
	v_mfma_f32_32x32x16_bf16 v[2:17], v[74:77], v[62:65], v[2:17]
	v_fma_f32 v158, v235, |v34|, v158
	v_fma_f32 v159, v235, |v35|, v159
	ds_read_b32 v235, v234
	s_waitcnt lgkmcnt(1)
	v_mfma_f32_32x32x16_bf16 v[2:17], v[78:81], v[58:61], v[2:17]
	v_mfma_f32_32x32x16_bf16 v[34:49], v[82:85], v[50:53], 0
	s_waitcnt lgkmcnt(0)
; #define LAS __attribute__((address_space(3)))
; #define IDX_ACC(cc, jj) do { float s0 = fmaf(wh, __builtin_fabsf(cc[0]), sacc[jj][0]); sacc[jj][0] = s0; \
;                             _Pragma("unroll") for (int r = 1; r < 16; ++r) { float a_ = sacc[jj][r]; asm("v_fma_f32 %0, %1, |%2|, %0" : "+v"(a_) : "v"(wh), "v"(cc[r]), "v"(s0)); sacc[jj][r] = a_; } } while (0)
; __global__ void __launch_bounds__(NTHREADS, 2) mega_fwd(Args args) {
;     ...
;                 for (int h = 0; h < NIH; ++h) {
;                     bf16x8 qf[4];
; #pragma unroll
;                     for (int ks = 0; ks < 4; ++ks) qf[ks] = *(const LAS bf16x8*)(Qs + (((h * 4 + ks) * 2 + hi5) * 32 + r32) * 16);
;                     const float wh = Ws[h * 32 + r32];
; #pragma unroll
;                     for (int jp = 0; jp < 4; jp += 2) { f32x16 c0 = f32x16{}, c1 = f32x16{};
; #pragma unroll
;                         for (int ks = 0; ks < 4; ++ks) { c0 = __builtin_amdgcn_mfma_f32_32x32x16_bf16(kf[jp][ks], qf[ks], c0, 0, 0, 0); c1 = __builtin_amdgcn_mfma_f32_32x32x16_bf16(kf[jp + 1][ks], qf[ks], c1, 0, 0, 0); }
;                         __builtin_amdgcn_sched_barrier(0);
;     ...
;                         IDX_ACC(c0, jp); IDX_ACC(c1, jp + 1);
;     ...
;                     }
;                 }
; #pragma unroll
;                 for (int j = 0; j < 4; ++j) { f32x16 c = f32x16{};
; #pragma unroll
;                     for (int ks = 0; ks < 4; ++ks) c = __builtin_amdgcn_mfma_f32_32x32x16_bf16(kf[j][ks], qlf[ks], c, 0, 0, 0);
; #pragma unroll
;                     for (int r = 0; r < 16; ++r) sacc[j][r] = 0.5f * (sacc[j][r] + c[r]); }
;                 float* srow = SCORES + (size_t)(q0 + r32) * S;
; #pragma unroll
;                 for (int j = 0; j < 4; ++j) if (kb0 + 32 * j < nadm) {
; #pragma unroll
;                     for (int rg = 0; rg < 4; ++rg) *(f32x4*)(srow + kb0 + 32 * j + 8 * rg + 4 * hi5) = (f32x4){sacc[j][4 * rg], sacc[j][4 * rg + 1], sacc[j][4 * rg + 2], sacc[j][4 * rg + 3]}; }
	s_nop 9
	v_fma_f32 v206, v235, |v2|, v206
	v_fma_f32 v207, v235, |v3|, v207
	v_fma_f32 v208, v235, |v4|, v208
	v_fma_f32 v209, v235, |v5|, v209
	v_fma_f32 v210, v235, |v6|, v210
	v_fma_f32 v211, v235, |v7|, v211
	v_fma_f32 v212, v235, |v8|, v212
	v_mfma_f32_32x32x16_bf16 v[34:49], v[86:89], v[54:57], v[34:49]
	v_fma_f32 v213, v235, |v9|, v213
	v_fma_f32 v214, v235, |v10|, v214
	v_fma_f32 v215, v235, |v11|, v215
	v_fma_f32 v216, v235, |v12|, v216
	v_fma_f32 v217, v235, |v13|, v217
	v_fma_f32 v218, v235, |v14|, v218
	v_fma_f32 v219, v235, |v15|, v219
	v_mfma_f32_32x32x16_bf16 v[18:33], v[98:101], v[50:53], 0
	v_fma_f32 v220, v235, |v16|, v220
	v_fma_f32 v221, v235, |v17|, v221
	v_mfma_f32_32x32x16_bf16 v[34:49], v[90:93], v[62:65], v[34:49]
	v_mfma_f32_32x32x16_bf16 v[18:33], v[102:105], v[54:57], v[18:33]
	v_mfma_f32_32x32x16_bf16 v[34:49], v[94:97], v[58:61], v[34:49]
	v_mfma_f32_32x32x16_bf16 v[18:33], v[106:109], v[62:65], v[18:33]
	s_nop 10
	v_fma_f32 v190, v235, |v34|, v190
	v_fma_f32 v191, v235, |v35|, v191
	v_fma_f32 v192, v235, |v36|, v192
	v_fma_f32 v193, v235, |v37|, v193
	v_fma_f32 v194, v235, |v38|, v194
	v_fma_f32 v195, v235, |v39|, v195
	v_fma_f32 v196, v235, |v40|, v196
	v_fma_f32 v197, v235, |v41|, v197
	v_fma_f32 v198, v235, |v42|, v198
	v_fma_f32 v199, v235, |v43|, v199
	v_fma_f32 v200, v235, |v44|, v200
	v_fma_f32 v201, v235, |v45|, v201
	v_fma_f32 v202, v235, |v46|, v202
	v_fma_f32 v203, v235, |v47|, v203
	v_fma_f32 v204, v235, |v48|, v204
	v_fma_f32 v205, v235, |v49|, v205
	v_mfma_f32_32x32x16_bf16 v[18:33], v[114:117], v[58:61], v[18:33]
	v_mfma_f32_32x32x16_bf16 v[2:17], v[130:133], v[50:53], 0
	s_addk_i32 s7, 0x2000
	s_nop 9
	v_fma_f32 v188, v235, |v18|, v188
	s_cmp_lg_u32 s7, 0x10000
	v_add_u32_e32 v234, 0x100, v234
	v_fma_f32 v189, v235, |v19|, v189
	v_fma_f32 v186, v235, |v20|, v186
	v_fma_f32 v187, v235, |v21|, v187
	v_mfma_f32_32x32x16_bf16 v[2:17], v[134:137], v[54:57], v[2:17]
	v_fma_f32 v184, v235, |v22|, v184
	v_fma_f32 v185, v235, |v23|, v185
	v_fma_f32 v182, v235, |v24|, v182
	v_fma_f32 v183, v235, |v25|, v183
	v_fma_f32 v180, v235, |v26|, v180
	v_fma_f32 v181, v235, |v27|, v181
	v_fma_f32 v178, v235, |v28|, v178
	v_mfma_f32_32x32x16_bf16 v[2:17], v[138:141], v[62:65], v[2:17]
	v_fma_f32 v179, v235, |v29|, v179
	v_fma_f32 v176, v235, |v30|, v176
	v_fma_f32 v177, v235, |v31|, v177
	v_fma_f32 v174, v235, |v32|, v174
	v_fma_f32 v175, v235, |v33|, v175
	v_mfma_f32_32x32x16_bf16 v[2:17], v[142:145], v[58:61], v[2:17]
	s_nop 11
	v_fma_f32 v172, v235, |v2|, v172
	v_fma_f32 v173, v235, |v3|, v173
	v_fma_f32 v170, v235, |v4|, v170
	v_fma_f32 v171, v235, |v5|, v171
	v_fma_f32 v168, v235, |v6|, v168
	v_fma_f32 v169, v235, |v7|, v169
	v_fma_f32 v166, v235, |v8|, v166
	v_fma_f32 v167, v235, |v9|, v167
	v_fma_f32 v164, v235, |v10|, v164
	v_fma_f32 v165, v235, |v11|, v165
	v_fma_f32 v162, v235, |v12|, v162
	v_fma_f32 v163, v235, |v13|, v163
	v_fma_f32 v160, v235, |v14|, v160
	v_fma_f32 v161, v235, |v15|, v161
	v_fma_f32 v158, v235, |v16|, v158
	v_fma_f32 v159, v235, |v17|, v159
	s_cbranch_scc1 .LBB0_656
	v_mfma_f32_32x32x16_bf16 v[50:65], v[66:69], v[110:113], 0
	v_lshlrev_b64 v[2:3], 15, v[156:157]
	v_lshl_add_u64 v[2:3], s[2:3], 0, v[2:3]
	s_ashr_i32 s7, s6, 31
	v_lshl_add_u64 v[2:3], s[6:7], 2, v[2:3]
	v_lshl_add_u64 v[156:157], v[2:3], 0, v[148:149]
	s_or_b32 s7, s6, 32
	s_cmp_ge_i32 s7, s28
	v_mfma_f32_32x32x16_bf16 v[34:49], v[82:85], v[110:113], 0
	v_mfma_f32_32x32x16_bf16 v[18:33], v[98:101], v[110:113], 0
	v_mfma_f32_32x32x16_bf16 v[2:17], v[130:133], v[110:113], 0
	v_mfma_f32_32x32x16_bf16 v[50:65], v[70:73], v[118:121], v[50:65]
	v_mfma_f32_32x32x16_bf16 v[34:49], v[86:89], v[118:121], v[34:49]
	v_mfma_f32_32x32x16_bf16 v[18:33], v[102:105], v[118:121], v[18:33]
	v_mfma_f32_32x32x16_bf16 v[2:17], v[134:137], v[118:121], v[2:17]
	v_mfma_f32_32x32x16_bf16 v[50:65], v[74:77], v[122:125], v[50:65]
	v_mfma_f32_32x32x16_bf16 v[34:49], v[90:93], v[122:125], v[34:49]
	v_mfma_f32_32x32x16_bf16 v[18:33], v[106:109], v[122:125], v[18:33]
	v_mfma_f32_32x32x16_bf16 v[2:17], v[138:141], v[122:125], v[2:17]
	v_mfma_f32_32x32x16_bf16 v[50:65], v[78:81], v[126:129], v[50:65]
	v_mfma_f32_32x32x16_bf16 v[34:49], v[94:97], v[126:129], v[34:49]
	s_nop 10
	v_add_f32_e64 v52, v52, v208
	v_add_f32_e64 v53, v53, v209
	v_add_f32_e64 v50, v50, v206
	v_add_f32_e64 v51, v51, v207
	v_add_f32_e64 v56, v56, v212
	v_add_f32_e64 v57, v57, v213
	v_pk_add_f32 v[54:55], v[54:55], v[210:211]
	v_pk_mul_f32 v[52:53], v[52:53], 0.5 op_sel_hi:[1,0]
	v_pk_mul_f32 v[50:51], v[50:51], 0.5 op_sel_hi:[1,0]
	v_pk_add_f32 v[60:61], v[60:61], v[216:217]
	v_mfma_f32_32x32x16_bf16 v[18:33], v[114:117], v[126:129], v[18:33]
	v_add_f32_e64 v58, v58, v214
	v_add_f32_e64 v59, v59, v215
	global_store_dwordx4 v[156:157], v[50:53], off
	v_add_f32_e64 v64, v64, v220
	v_add_f32_e64 v65, v65, v221
	v_pk_add_f32 v[62:63], v[62:63], v[218:219]
	v_pk_mul_f32 v[52:53], v[56:57], 0.5 op_sel_hi:[1,0]
	v_pk_mul_f32 v[50:51], v[54:55], 0.5 op_sel_hi:[1,0]
	global_store_dwordx4 v[156:157], v[50:53], off offset:32
	v_mfma_f32_32x32x16_bf16 v[2:17], v[142:145], v[126:129], v[2:17]
	s_nop 0
	v_mul_f32_e64 v52, v60, 0.5
	v_mul_f32_e64 v53, v61, 0.5
	v_mul_f32_e64 v50, v58, 0.5
	v_mul_f32_e64 v51, v59, 0.5
	global_store_dwordx4 v[156:157], v[50:53], off offset:64
	s_nop 1
	v_pk_mul_f32 v[52:53], v[64:65], 0.5 op_sel_hi:[1,0]
	v_pk_mul_f32 v[50:51], v[62:63], 0.5 op_sel_hi:[1,0]
	global_store_dwordx4 v[156:157], v[50:53], off offset:96
	s_cbranch_scc1 .LBB0_663
	v_pk_add_f32 v[36:37], v[36:37], v[192:193]
	v_pk_add_f32 v[34:35], v[34:35], v[190:191]
	v_pk_add_f32 v[40:41], v[40:41], v[196:197]
	v_pk_add_f32 v[38:39], v[38:39], v[194:195]
	v_pk_mul_f32 v[36:37], v[36:37], 0.5 op_sel_hi:[1,0]
	v_pk_mul_f32 v[34:35], v[34:35], 0.5 op_sel_hi:[1,0]
	v_pk_add_f32 v[44:45], v[44:45], v[200:201]
	v_pk_add_f32 v[42:43], v[42:43], v[198:199]
	global_store_dwordx4 v[156:157], v[34:37], off offset:128
	v_pk_add_f32 v[48:49], v[48:49], v[204:205]
	v_pk_add_f32 v[46:47], v[46:47], v[202:203]
	v_pk_mul_f32 v[36:37], v[40:41], 0.5 op_sel_hi:[1,0]
	v_pk_mul_f32 v[34:35], v[38:39], 0.5 op_sel_hi:[1,0]
	global_store_dwordx4 v[156:157], v[34:37], off offset:160
	s_nop 1
	v_pk_mul_f32 v[36:37], v[44:45], 0.5 op_sel_hi:[1,0]
	v_pk_mul_f32 v[34:35], v[42:43], 0.5 op_sel_hi:[1,0]
	global_store_dwordx4 v[156:157], v[34:37], off offset:192
	s_nop 1
	v_pk_mul_f32 v[36:37], v[48:49], 0.5 op_sel_hi:[1,0]
	v_pk_mul_f32 v[34:35], v[46:47], 0.5 op_sel_hi:[1,0]
	global_store_dwordx4 v[156:157], v[34:37], off offset:224
	s_or_b32 s7, s6, 64
	s_cmp_ge_i32 s7, s28
	s_cbranch_scc0 .LBB0_664
